# QKV: sc1 stores only in the last unit of each workgroup (on v40)
# baseline (speedup 1.0000x reference)
.LBB3_21:
	s_cmp_lt_u32 s60, 8
	s_mul_i32 s23, s60, 0x300
	s_cselect_b32 s20, 8, 16
	s_cmp_gt_u32 s60, 3
	v_add_u32_e32 v58, s23, v92
	s_cselect_b32 s20, s20, 0
	ds_read_b128 v[72:75], v58
	ds_read_b128 v[76:79], v58 offset:16
	v_add_u32_e32 v58, v58, v93
	s_add_u32 s20, s0, s20
	ds_read_b128 v[98:101], v58 offset:128
	s_addc_u32 s21, s1, 0
	s_and_b32 s22, s60, 3
	s_mulk_i32 s22, 0xc0
	s_add_i32 s22, s22, s51
	v_add_u32_e32 v104, s22, v83
	s_waitcnt lgkmcnt(0)
	v_pk_add_f32 v[44:45], v[44:45], v[72:73]
	v_pk_add_f32 v[32:33], v[32:33], v[72:73]
	v_pk_add_f32 v[20:21], v[20:21], v[72:73]
	v_pk_add_f32 v[8:9], v[8:9], v[72:73]
	s_add_i32 s22, s22, 32
	v_pk_add_f32 v[102:103], v[36:37], v[98:99]
	v_cvt_pk_f16_f32 v36, v44, v45
	v_pk_add_f32 v[44:45], v[24:25], v[98:99]
	v_cvt_pk_f16_f32 v24, v32, v33
	v_pk_add_f32 v[32:33], v[12:13], v[98:99]
	v_cvt_pk_f16_f32 v12, v20, v21
	v_pk_add_f32 v[20:21], v[0:1], v[98:99]
	v_cvt_pk_f16_f32 v0, v8, v9
	s_lshr_b32 s23, s22, 6
	v_and_or_b32 v8, s22, 48, v84
	s_lshl_b32 s22, s55, 7
	s_add_i32 s22, s22, s50
	s_ashr_i32 s24, s22, 12
	s_bfe_u32 s22, s22, 0x60006
	s_mul_i32 s25, s22, 37
	s_lshr_b32 s25, s25, 9
	s_load_dwordx2 s[20:21], s[20:21], 0x28
	s_mul_i32 s26, s25, -14
	s_add_i32 s26, s26, s22
	s_mul_i32 s24, s24, 25
	s_mul_i32 s22, s25, 5
	v_pk_add_f32 v[42:43], v[42:43], v[78:79]
	v_pk_add_f32 v[30:31], v[30:31], v[78:79]
	v_pk_add_f32 v[18:19], v[18:19], v[78:79]
	v_pk_add_f32 v[10:11], v[10:11], v[74:75]
	v_pk_add_f32 v[6:7], v[6:7], v[78:79]
	s_add_i32 s22, s22, s24
	v_pk_add_f32 v[80:81], v[38:39], v[100:101]
	v_cvt_pk_f16_f32 v39, v42, v43
	v_pk_add_f32 v[42:43], v[26:27], v[100:101]
	v_cvt_pk_f16_f32 v27, v30, v31
	v_pk_add_f32 v[30:31], v[14:15], v[100:101]
	v_cvt_pk_f16_f32 v15, v18, v19
	v_pk_add_f32 v[4:5], v[4:5], v[76:77]
	v_pk_add_f32 v[18:19], v[2:3], v[100:101]
	v_cvt_pk_f16_f32 v1, v10, v11
	v_cvt_pk_f16_f32 v3, v6, v7
	v_and_b32_e32 v6, 56, v104
	v_add_u32_e32 v11, s22, v85
	v_sub_u32_e32 v10, s26, v85
	v_cvt_pk_f16_f32 v2, v4, v5
	v_cvt_pk_f16_f32 v4, v20, v21
	v_lshrrev_b32_e32 v20, 6, v104
	v_lshlrev_b32_e32 v58, 1, v6
	v_mad_i32_i24 v10, v10, 14, v82
	v_mul_lo_u32 v21, v11, 12
	v_cvt_pk_f16_f32 v5, v18, v19
	s_waitcnt lgkmcnt(0)
	v_lshl_add_u64 v[6:7], s[20:21], 0, v[58:59]
	v_lshlrev_b32_e32 v58, 1, v8
	v_add_u32_e32 v18, v21, v20
	v_ashrrev_i32_e32 v11, 31, v10
	v_lshl_add_u64 v[8:9], s[20:21], 0, v[58:59]
	v_mad_i64_i32 v[18:19], s[20:21], v18, s59, v[10:11]
	v_pk_add_f32 v[46:47], v[46:47], v[74:75]
	v_pk_add_f32 v[40:41], v[40:41], v[76:77]
	v_lshlrev_b64 v[18:19], 7, v[18:19]
	v_cvt_pk_f16_f32 v37, v46, v47
	v_cvt_pk_f16_f32 v38, v40, v41
	v_lshl_add_u64 v[18:19], v[6:7], 0, v[18:19]
	s_cmp_eq_u64 s[8:9], 0
	s_cbranch_scc1 .Lq_plain_0
	global_store_dwordx4 v[18:19], v[36:39], off sc1
	s_branch .Lq_join_0
.Lq_plain_0:
	global_store_dwordx4 v[18:19], v[36:39], off
.Lq_join_0:
	v_add_u32_e32 v18, s23, v21
	v_mad_i64_i32 v[10:11], s[20:21], v18, s59, v[10:11]
	v_lshlrev_b64 v[10:11], 7, v[10:11]
	v_cvt_pk_f16_f32 v40, v102, v103
	v_cvt_pk_f16_f32 v41, v80, v81
	v_lshl_add_u64 v[10:11], v[8:9], 0, v[10:11]
	s_cmp_eq_u64 s[8:9], 0
	s_cbranch_scc1 .Lq_plain_1
	global_store_dwordx2 v[10:11], v[40:41], off sc1
	s_branch .Lq_join_1
.Lq_plain_1:
	global_store_dwordx2 v[10:11], v[40:41], off
.Lq_join_1:
	v_add_u32_e32 v11, s22, v87
	v_sub_u32_e32 v10, s26, v87
	v_mad_i32_i24 v10, v10, 14, v86
	v_mul_lo_u32 v21, v11, 12
	v_add_u32_e32 v18, v21, v20
	v_ashrrev_i32_e32 v11, 31, v10
	v_mad_i64_i32 v[18:19], s[20:21], v18, s59, v[10:11]
	v_pk_add_f32 v[34:35], v[34:35], v[74:75]
	v_pk_add_f32 v[28:29], v[28:29], v[76:77]
	v_lshlrev_b64 v[18:19], 7, v[18:19]
	v_cvt_pk_f16_f32 v25, v34, v35
	v_cvt_pk_f16_f32 v26, v28, v29
	v_lshl_add_u64 v[18:19], v[6:7], 0, v[18:19]
	s_cmp_eq_u64 s[8:9], 0
	s_cbranch_scc1 .Lq_plain_2
	global_store_dwordx4 v[18:19], v[24:27], off sc1
	s_branch .Lq_join_2
.Lq_plain_2:
	global_store_dwordx4 v[18:19], v[24:27], off
.Lq_join_2:
	v_add_u32_e32 v18, s23, v21
	v_mad_i64_i32 v[10:11], s[20:21], v18, s59, v[10:11]
	v_lshlrev_b64 v[10:11], 7, v[10:11]
	v_cvt_pk_f16_f32 v28, v44, v45
	v_cvt_pk_f16_f32 v29, v42, v43
	v_lshl_add_u64 v[10:11], v[8:9], 0, v[10:11]
	s_cmp_eq_u64 s[8:9], 0
	s_cbranch_scc1 .Lq_plain_3
	global_store_dwordx2 v[10:11], v[28:29], off sc1
	s_branch .Lq_join_3
.Lq_plain_3:
	global_store_dwordx2 v[10:11], v[28:29], off
.Lq_join_3:
	v_add_u32_e32 v11, s22, v89
	v_sub_u32_e32 v10, s26, v89
	v_mad_i32_i24 v10, v10, 14, v88
	v_mul_lo_u32 v21, v11, 12
	v_add_u32_e32 v18, v21, v20
	v_ashrrev_i32_e32 v11, 31, v10
	v_mad_i64_i32 v[18:19], s[20:21], v18, s59, v[10:11]
	v_pk_add_f32 v[22:23], v[22:23], v[74:75]
	v_pk_add_f32 v[16:17], v[16:17], v[76:77]
	v_lshlrev_b64 v[18:19], 7, v[18:19]
	v_cvt_pk_f16_f32 v13, v22, v23
	v_cvt_pk_f16_f32 v14, v16, v17
	v_lshl_add_u64 v[18:19], v[6:7], 0, v[18:19]
	s_cmp_eq_u64 s[8:9], 0
	s_cbranch_scc1 .Lq_plain_4
	global_store_dwordx4 v[18:19], v[12:15], off sc1
	s_branch .Lq_join_4
.Lq_plain_4:
	global_store_dwordx4 v[18:19], v[12:15], off
.Lq_join_4:
	v_cvt_pk_f16_f32 v16, v32, v33
	v_cvt_pk_f16_f32 v17, v30, v31
	v_add_u32_e32 v12, s23, v21
	v_mad_i64_i32 v[10:11], s[20:21], v12, s59, v[10:11]
	v_lshlrev_b64 v[10:11], 7, v[10:11]
	v_lshl_add_u64 v[10:11], v[8:9], 0, v[10:11]
	s_cmp_eq_u64 s[8:9], 0
	s_cbranch_scc1 .Lq_plain_5
	global_store_dwordx2 v[10:11], v[16:17], off sc1
	s_branch .Lq_join_5
.Lq_plain_5:
	global_store_dwordx2 v[10:11], v[16:17], off
.Lq_join_5:
	v_add_u32_e32 v11, s22, v91
	v_sub_u32_e32 v10, s26, v91
	v_mad_i32_i24 v10, v10, 14, v90
	v_mul_lo_u32 v14, v11, 12
	v_add_u32_e32 v12, v14, v20
	v_ashrrev_i32_e32 v11, 31, v10
	v_mad_i64_i32 v[12:13], s[20:21], v12, s59, v[10:11]
	v_lshlrev_b64 v[12:13], 7, v[12:13]
	v_lshl_add_u64 v[6:7], v[6:7], 0, v[12:13]
	s_cmp_eq_u64 s[8:9], 0
	s_cbranch_scc1 .Lq_plain_6
	global_store_dwordx4 v[6:7], v[0:3], off sc1
	s_branch .Lq_join_6
.Lq_plain_6:
	global_store_dwordx4 v[6:7], v[0:3], off
.Lq_join_6:
	s_and_b64 vcc, exec, s[8:9]
	s_mov_b32 s60, s61
	v_add_u32_e32 v0, s23, v14
	v_mad_i64_i32 v[0:1], s[20:21], v0, s59, v[10:11]
	v_lshlrev_b64 v[0:1], 7, v[0:1]
	v_lshl_add_u64 v[0:1], v[8:9], 0, v[0:1]
	s_mov_b32 s55, s62
	s_mov_b64 s[22:23], s[6:7]
	s_mov_b64 s[20:21], s[4:5]
	s_cmp_eq_u64 s[8:9], 0
	s_cbranch_scc1 .Lq_plain_7
	global_store_dwordx2 v[0:1], v[4:5], off sc1
	s_branch .Lq_join_7
.Lq_plain_7:
	global_store_dwordx2 v[0:1], v[4:5], off
.Lq_join_7:
	s_cbranch_vccnz .LBB3_35
